# K-loop load segments: tile LDS-DMA issued before the ds_read block (P1 all, P6/P10 3 of 4, P9 2 of 4 sub-phases) for earlier DMA start
# baseline (speedup 1.0000x reference)
; template <class Epi, bool GATHER, bool EXPERT, bool FP8>
; DI void gemm_phase(LAS unsigned char* lds, const Gemm g, const StaticOrder& S, const Epi& E) {
;     ...
;         for (int t = 0; t < nt; t += 2) {
;             const bool last = (t == nt - 2);
;             const char* a1 = cA + (size_t)(t + 1) * kstep;
;             const char* a2 = last ? nA : cA + (size_t)(t + 2) * kstep; const char* b2 = last ? nB : cB + (size_t)(t + 2) * kstep;
;             const char* a3 = a2 + kstep; const char* b3 = b2 + kstep;
;             unsigned o00 = coffA[0][0], o01 = coffA[0][1], o10 = coffA[1][0], o11 = coffA[1][1];
;             if (GATHER && last && has_next) {
;                 o00 = sp[0] * (unsigned)(K * 2) + (unsigned)C0x2; o01 = sp[512] * (unsigned)(K * 2) + (unsigned)C1x2;
;                 o10 = sp[1024] * (unsigned)(K * 2) + (unsigned)C0x2; o11 = sp[1536] * (unsigned)(K * 2) + (unsigned)C1x2; }
;             PG8_TRIP(a1, a2, b2, a3, b3, o00, o01, o10, o11);
.LBB0_115:
	s_add_u32 s0, s6, 0x80
	s_addc_u32 s1, s7, 0
	s_cmp_eq_u32 s18, 28
	s_cselect_b32 s9, s43, s1
	s_cselect_b32 s8, s42, s0
	s_cselect_b32 s1, s45, s15
	s_cselect_b32 s0, s44, s5
	v_mov_b32_e32 v186, v227
	s_add_i32 m0, s37, 0xc000
	s_nop 0
	global_load_lds_dwordx4 v186, s[6:7]
	v_mov_b32_e32 v186, v229
	s_add_i32 m0, s37, 0xe000
	s_nop 0
	global_load_lds_dwordx4 v186, s[6:7]
	ds_read_b128 v[130:133], v231
	ds_read_b128 v[134:137], v231 offset:1024
	ds_read_b128 v[138:141], v231 offset:2048
	ds_read_b128 v[142:145], v231 offset:3072
	ds_read_b128 v[146:149], v232
	ds_read_b128 v[150:153], v232 offset:1024
	ds_read_b128 v[154:157], v232 offset:2048
	ds_read_b128 v[158:161], v232 offset:3072
	ds_read_b128 v[162:165], v233
	ds_read_b128 v[166:169], v233 offset:1024
	ds_read_b128 v[170:173], v233 offset:2048
	ds_read_b128 v[174:177], v233 offset:3072
	ds_read_b128 v[178:181], v233 offset:4096
	ds_read_b128 v[182:185], v233 offset:5120
	ds_read_b128 v[192:195], v233 offset:6144
	ds_read_b128 v[196:199], v233 offset:7168
	s_waitcnt vmcnt(8)
	s_waitcnt lgkmcnt(0)
	s_barrier
	s_setprio 1
	s_waitcnt lgkmcnt(0)
	v_mfma_f32_16x16x32_bf16 v[126:129], v[130:133], v[162:165], v[126:129]
	v_mfma_f32_16x16x32_bf16 v[122:125], v[138:141], v[162:165], v[122:125]
	v_mfma_f32_16x16x32_bf16 v[118:121], v[130:133], v[170:173], v[118:121]
	v_mfma_f32_16x16x32_bf16 v[110:113], v[138:141], v[170:173], v[110:113]
	v_mfma_f32_16x16x32_bf16 v[102:105], v[130:133], v[178:181], v[102:105]
	v_mfma_f32_16x16x32_bf16 v[94:97], v[138:141], v[178:181], v[94:97]
	v_mfma_f32_16x16x32_bf16 v[86:89], v[130:133], v[192:195], v[86:89]
	v_mfma_f32_16x16x32_bf16 v[78:81], v[138:141], v[192:195], v[78:81]
	v_mfma_f32_16x16x32_bf16 v[126:129], v[134:137], v[166:169], v[126:129]
	v_mfma_f32_16x16x32_bf16 v[122:125], v[142:145], v[166:169], v[122:125]
	v_mfma_f32_16x16x32_bf16 v[118:121], v[134:137], v[174:177], v[118:121]
	v_mfma_f32_16x16x32_bf16 v[110:113], v[142:145], v[174:177], v[110:113]
	v_mfma_f32_16x16x32_bf16 v[102:105], v[134:137], v[182:185], v[102:105]
	v_mfma_f32_16x16x32_bf16 v[94:97], v[142:145], v[182:185], v[94:97]
	v_mfma_f32_16x16x32_bf16 v[86:89], v[134:137], v[196:199], v[86:89]
	v_mfma_f32_16x16x32_bf16 v[78:81], v[142:145], v[196:199], v[78:81]
	s_setprio 0
	s_setprio 1
	v_mfma_f32_16x16x32_bf16 v[114:117], v[146:149], v[162:165], v[114:117]
	v_mfma_f32_16x16x32_bf16 v[106:109], v[154:157], v[162:165], v[106:109]
	v_mfma_f32_16x16x32_bf16 v[98:101], v[146:149], v[170:173], v[98:101]
	v_mfma_f32_16x16x32_bf16 v[90:93], v[154:157], v[170:173], v[90:93]
	v_mfma_f32_16x16x32_bf16 v[82:85], v[146:149], v[178:181], v[82:85]
	v_mfma_f32_16x16x32_bf16 v[74:77], v[154:157], v[178:181], v[74:77]
	v_mfma_f32_16x16x32_bf16 v[70:73], v[146:149], v[192:195], v[70:73]
	v_mfma_f32_16x16x32_bf16 v[66:69], v[154:157], v[192:195], v[66:69]
	v_mfma_f32_16x16x32_bf16 v[114:117], v[150:153], v[166:169], v[114:117]
	v_mfma_f32_16x16x32_bf16 v[106:109], v[158:161], v[166:169], v[106:109]
	v_mfma_f32_16x16x32_bf16 v[98:101], v[150:153], v[174:177], v[98:101]
	v_mfma_f32_16x16x32_bf16 v[90:93], v[158:161], v[174:177], v[90:93]
	v_mfma_f32_16x16x32_bf16 v[82:85], v[150:153], v[182:185], v[82:85]
	v_mfma_f32_16x16x32_bf16 v[74:77], v[158:161], v[182:185], v[74:77]
	v_mfma_f32_16x16x32_bf16 v[70:73], v[150:153], v[196:199], v[70:73]
	v_mfma_f32_16x16x32_bf16 v[66:69], v[158:161], v[196:199], v[66:69]
	s_setprio 0
	s_barrier
	v_mov_b32_e32 v186, v1
	s_add_i32 s33, s75, s53
	s_mov_b32 m0, s33
	s_nop 0
	global_load_lds_dwordx4 v186, s[0:1]
	v_mov_b32_e32 v186, v225
	s_add_i32 m0, s33, 0x2000
	s_add_u32 s46, s0, 0x80000
	global_load_lds_dwordx4 v186, s[0:1]
	s_addc_u32 s47, s1, 0
	v_mov_b32_e32 v186, v1
	s_add_i32 s33, s76, s53
	s_mov_b32 m0, s33
	s_nop 0
	global_load_lds_dwordx4 v186, s[46:47]
	v_mov_b32_e32 v186, v225
	s_add_i32 m0, s33, 0x2000
	s_nop 0
	global_load_lds_dwordx4 v186, s[46:47]
	v_mov_b32_e32 v186, v226
	s_mov_b32 m0, s37
	s_nop 0
	global_load_lds_dwordx4 v186, s[8:9]
	v_mov_b32_e32 v186, v228
	s_mov_b32 m0, s54
	s_nop 0
	global_load_lds_dwordx4 v186, s[8:9]
	ds_read_b128 v[162:165], v233 offset:16384
	ds_read_b128 v[166:169], v233 offset:17408
	ds_read_b128 v[170:173], v233 offset:18432
	ds_read_b128 v[174:177], v233 offset:19456
	ds_read_b128 v[178:181], v233 offset:20480
	ds_read_b128 v[182:185], v233 offset:21504
	ds_read_b128 v[192:195], v233 offset:22528
	ds_read_b128 v[196:199], v233 offset:23552
	s_waitcnt vmcnt(8)
	s_waitcnt lgkmcnt(0)
	s_barrier
	s_setprio 1
	s_waitcnt lgkmcnt(0)
	v_mfma_f32_16x16x32_bf16 v[62:65], v[130:133], v[162:165], v[62:65]
	v_mfma_f32_16x16x32_bf16 v[58:61], v[138:141], v[162:165], v[58:61]
	v_mfma_f32_16x16x32_bf16 v[54:57], v[130:133], v[170:173], v[54:57]
	v_mfma_f32_16x16x32_bf16 v[46:49], v[138:141], v[170:173], v[46:49]
	v_mfma_f32_16x16x32_bf16 v[38:41], v[130:133], v[178:181], v[38:41]
	v_mfma_f32_16x16x32_bf16 v[30:33], v[138:141], v[178:181], v[30:33]
	v_mfma_f32_16x16x32_bf16 v[22:25], v[130:133], v[192:195], v[22:25]
	v_mfma_f32_16x16x32_bf16 v[14:17], v[138:141], v[192:195], v[14:17]
	v_mfma_f32_16x16x32_bf16 v[62:65], v[134:137], v[166:169], v[62:65]
	v_mfma_f32_16x16x32_bf16 v[58:61], v[142:145], v[166:169], v[58:61]
	v_mfma_f32_16x16x32_bf16 v[54:57], v[134:137], v[174:177], v[54:57]
	v_mfma_f32_16x16x32_bf16 v[46:49], v[142:145], v[174:177], v[46:49]
	v_mfma_f32_16x16x32_bf16 v[38:41], v[134:137], v[182:185], v[38:41]
	v_mfma_f32_16x16x32_bf16 v[30:33], v[142:145], v[182:185], v[30:33]
	v_mfma_f32_16x16x32_bf16 v[22:25], v[134:137], v[196:199], v[22:25]
	v_mfma_f32_16x16x32_bf16 v[14:17], v[142:145], v[196:199], v[14:17]
	s_setprio 0
	s_setprio 1
	v_mfma_f32_16x16x32_bf16 v[50:53], v[146:149], v[162:165], v[50:53]
	v_mfma_f32_16x16x32_bf16 v[42:45], v[154:157], v[162:165], v[42:45]
	v_mfma_f32_16x16x32_bf16 v[34:37], v[146:149], v[170:173], v[34:37]
	v_mfma_f32_16x16x32_bf16 v[26:29], v[154:157], v[170:173], v[26:29]
	v_mfma_f32_16x16x32_bf16 v[18:21], v[146:149], v[178:181], v[18:21]
	v_mfma_f32_16x16x32_bf16 v[10:13], v[154:157], v[178:181], v[10:13]
	v_mfma_f32_16x16x32_bf16 v[6:9], v[146:149], v[192:195], v[6:9]
	v_mfma_f32_16x16x32_bf16 v[2:5], v[154:157], v[192:195], v[2:5]
	v_mfma_f32_16x16x32_bf16 v[50:53], v[150:153], v[166:169], v[50:53]
	v_mfma_f32_16x16x32_bf16 v[42:45], v[158:161], v[166:169], v[42:45]
	v_mfma_f32_16x16x32_bf16 v[34:37], v[150:153], v[174:177], v[34:37]
	v_mfma_f32_16x16x32_bf16 v[26:29], v[158:161], v[174:177], v[26:29]
	v_mfma_f32_16x16x32_bf16 v[18:21], v[150:153], v[182:185], v[18:21]
	v_mfma_f32_16x16x32_bf16 v[10:13], v[158:161], v[182:185], v[10:13]
	v_mfma_f32_16x16x32_bf16 v[6:9], v[150:153], v[196:199], v[6:9]
	v_mfma_f32_16x16x32_bf16 v[2:5], v[158:161], v[196:199], v[2:5]
	s_setprio 0
	s_barrier
	s_add_i32 s33, 0, 0x18000
	s_add_i32 s39, 0, 0x1c000
	v_add_u32_e32 v142, s33, v230
	v_add_u32_e32 v158, s39, v230
	v_mov_b32_e32 v186, v227
	s_mov_b32 m0, s55
	s_nop 0
	global_load_lds_dwordx4 v186, s[8:9]
	v_mov_b32_e32 v186, v229
	s_mov_b32 m0, s56
	s_nop 0
	global_load_lds_dwordx4 v186, s[8:9]
	ds_read_b128 v[130:133], v142
	ds_read_b128 v[134:137], v142 offset:1024
	ds_read_b128 v[138:141], v142 offset:2048
	ds_read_b128 v[142:145], v142 offset:3072
	ds_read_b128 v[146:149], v158
	ds_read_b128 v[150:153], v158 offset:1024
	ds_read_b128 v[154:157], v158 offset:2048
	ds_read_b128 v[158:161], v158 offset:3072
	ds_read_b128 v[162:165], v233 offset:32768
	ds_read_b128 v[166:169], v233 offset:33792
	ds_read_b128 v[170:173], v233 offset:34816
	ds_read_b128 v[174:177], v233 offset:35840
	ds_read_b128 v[178:181], v233 offset:36864
	ds_read_b128 v[182:185], v233 offset:37888
	ds_read_b128 v[192:195], v233 offset:38912
	ds_read_b128 v[196:199], v233 offset:39936
	s_waitcnt vmcnt(8)
	s_waitcnt lgkmcnt(0)
	s_barrier
	s_setprio 1
	s_waitcnt lgkmcnt(0)
	v_mfma_f32_16x16x32_bf16 v[126:129], v[130:133], v[162:165], v[126:129]
	v_mfma_f32_16x16x32_bf16 v[122:125], v[138:141], v[162:165], v[122:125]
	v_mfma_f32_16x16x32_bf16 v[118:121], v[130:133], v[170:173], v[118:121]
	v_mfma_f32_16x16x32_bf16 v[110:113], v[138:141], v[170:173], v[110:113]
	v_mfma_f32_16x16x32_bf16 v[102:105], v[130:133], v[178:181], v[102:105]
	v_mfma_f32_16x16x32_bf16 v[94:97], v[138:141], v[178:181], v[94:97]
	v_mfma_f32_16x16x32_bf16 v[86:89], v[130:133], v[192:195], v[86:89]
	v_mfma_f32_16x16x32_bf16 v[78:81], v[138:141], v[192:195], v[78:81]
	v_mfma_f32_16x16x32_bf16 v[126:129], v[134:137], v[166:169], v[126:129]
	v_mfma_f32_16x16x32_bf16 v[122:125], v[142:145], v[166:169], v[122:125]
	v_mfma_f32_16x16x32_bf16 v[118:121], v[134:137], v[174:177], v[118:121]
	v_mfma_f32_16x16x32_bf16 v[110:113], v[142:145], v[174:177], v[110:113]
	v_mfma_f32_16x16x32_bf16 v[102:105], v[134:137], v[182:185], v[102:105]
	v_mfma_f32_16x16x32_bf16 v[94:97], v[142:145], v[182:185], v[94:97]
	v_mfma_f32_16x16x32_bf16 v[86:89], v[134:137], v[196:199], v[86:89]
	v_mfma_f32_16x16x32_bf16 v[78:81], v[142:145], v[196:199], v[78:81]
	s_setprio 0
	s_setprio 1
	v_mfma_f32_16x16x32_bf16 v[114:117], v[146:149], v[162:165], v[114:117]
	v_mfma_f32_16x16x32_bf16 v[106:109], v[154:157], v[162:165], v[106:109]
	v_mfma_f32_16x16x32_bf16 v[98:101], v[146:149], v[170:173], v[98:101]
	v_mfma_f32_16x16x32_bf16 v[90:93], v[154:157], v[170:173], v[90:93]
	v_mfma_f32_16x16x32_bf16 v[82:85], v[146:149], v[178:181], v[82:85]
	v_mfma_f32_16x16x32_bf16 v[74:77], v[154:157], v[178:181], v[74:77]
	v_mfma_f32_16x16x32_bf16 v[70:73], v[146:149], v[192:195], v[70:73]
	v_mfma_f32_16x16x32_bf16 v[66:69], v[154:157], v[192:195], v[66:69]
	v_mfma_f32_16x16x32_bf16 v[114:117], v[150:153], v[166:169], v[114:117]
	v_mfma_f32_16x16x32_bf16 v[106:109], v[158:161], v[166:169], v[106:109]
	v_mfma_f32_16x16x32_bf16 v[98:101], v[150:153], v[174:177], v[98:101]
	v_mfma_f32_16x16x32_bf16 v[90:93], v[158:161], v[174:177], v[90:93]
	v_mfma_f32_16x16x32_bf16 v[82:85], v[150:153], v[182:185], v[82:85]
	v_mfma_f32_16x16x32_bf16 v[74:77], v[158:161], v[182:185], v[74:77]
	v_mfma_f32_16x16x32_bf16 v[70:73], v[150:153], v[196:199], v[70:73]
	v_mfma_f32_16x16x32_bf16 v[66:69], v[158:161], v[196:199], v[66:69]
	s_setprio 0
	s_barrier
; template <class Epi, bool GATHER, bool EXPERT, bool FP8>
; DI void gemm_phase(LAS unsigned char* lds, const Gemm g, const StaticOrder& S, const Epi& E) {
;     ...
;         for (int t = 0; t < nt; t += 2) {
;             const bool last = (t == nt - 2);
;             const char* a1 = cA + (size_t)(t + 1) * kstep;
;             const char* a2 = last ? nA : cA + (size_t)(t + 2) * kstep; const char* b2 = last ? nB : cB + (size_t)(t + 2) * kstep;
;             const char* a3 = a2 + kstep; const char* b3 = b2 + kstep;
;             unsigned o00 = coffA[0][0], o01 = coffA[0][1], o10 = coffA[1][0], o11 = coffA[1][1];
;             if (GATHER && last && has_next) {
;                 o00 = sp[0] * (unsigned)(K * 2) + (unsigned)C0x2; o01 = sp[512] * (unsigned)(K * 2) + (unsigned)C1x2;
;                 o10 = sp[1024] * (unsigned)(K * 2) + (unsigned)C0x2; o11 = sp[1536] * (unsigned)(K * 2) + (unsigned)C1x2; }
;             PG8_TRIP(a1, a2, b2, a3, b3, o00, o01, o10, o11);
;             if (last) { coffA[0][0] = o00; coffA[0][1] = o01; coffA[1][0] = o10; coffA[1][1] = o11; }
;         }
	v_mov_b32_e32 v186, v1
	s_add_i32 s33, s33, s53
	v_lshl_add_u64 v[200:201], s[0:1], 0, v[186:187]
	v_lshl_add_u64 v[200:201], v[200:201], 0, s[24:25]
	s_mov_b32 m0, s33
	v_mov_b32_e32 v186, v225
	global_load_lds_dwordx4 v[200:201], off
	s_add_i32 m0, s33, 0x2000
	s_nop 0
	v_lshl_add_u64 v[200:201], s[0:1], 0, v[186:187]
	s_add_u32 s0, s0, 0x80080
	v_lshl_add_u64 v[200:201], v[200:201], 0, s[24:25]
	s_addc_u32 s1, s1, 0
	v_mov_b32_e32 v186, v1
	s_add_i32 s33, s39, s53
	global_load_lds_dwordx4 v[200:201], off
	s_mov_b32 m0, s33
	s_nop 0
	global_load_lds_dwordx4 v186, s[0:1]
	v_mov_b32_e32 v186, v225
	s_add_i32 m0, s33, 0x2000
	s_nop 0
	global_load_lds_dwordx4 v186, s[0:1]
	v_mov_b32_e32 v186, v226
	s_mov_b32 m0, s62
	v_lshl_add_u64 v[200:201], s[8:9], 0, v[186:187]
	v_lshl_add_u64 v[200:201], v[200:201], 0, s[24:25]
	v_mov_b32_e32 v186, v228
	global_load_lds_dwordx4 v[200:201], off
	s_mov_b32 m0, s63
	v_lshl_add_u64 v[200:201], s[8:9], 0, v[186:187]
	v_lshl_add_u64 v[200:201], v[200:201], 0, s[24:25]
	global_load_lds_dwordx4 v[200:201], off
	ds_read_b128 v[162:165], v233 offset:49152
	ds_read_b128 v[166:169], v233 offset:50176
	ds_read_b128 v[170:173], v233 offset:51200
	ds_read_b128 v[174:177], v233 offset:52224
	ds_read_b128 v[178:181], v233 offset:53248
	ds_read_b128 v[182:185], v233 offset:54272
	ds_read_b128 v[192:195], v233 offset:55296
	ds_read_b128 v[196:199], v233 offset:56320
	s_waitcnt vmcnt(8)
	s_waitcnt lgkmcnt(0)
	s_barrier
	s_setprio 1
	s_waitcnt lgkmcnt(0)
	v_mfma_f32_16x16x32_bf16 v[62:65], v[130:133], v[162:165], v[62:65]
	v_mfma_f32_16x16x32_bf16 v[58:61], v[138:141], v[162:165], v[58:61]
	v_mfma_f32_16x16x32_bf16 v[54:57], v[130:133], v[170:173], v[54:57]
	v_mfma_f32_16x16x32_bf16 v[46:49], v[138:141], v[170:173], v[46:49]
	v_mfma_f32_16x16x32_bf16 v[38:41], v[130:133], v[178:181], v[38:41]
	v_mfma_f32_16x16x32_bf16 v[30:33], v[138:141], v[178:181], v[30:33]
	v_mfma_f32_16x16x32_bf16 v[22:25], v[130:133], v[192:195], v[22:25]
	v_mfma_f32_16x16x32_bf16 v[14:17], v[138:141], v[192:195], v[14:17]
	v_mfma_f32_16x16x32_bf16 v[62:65], v[134:137], v[166:169], v[62:65]
	v_mfma_f32_16x16x32_bf16 v[58:61], v[142:145], v[166:169], v[58:61]
	v_mfma_f32_16x16x32_bf16 v[54:57], v[134:137], v[174:177], v[54:57]
	v_mfma_f32_16x16x32_bf16 v[46:49], v[142:145], v[174:177], v[46:49]
	v_mfma_f32_16x16x32_bf16 v[38:41], v[134:137], v[182:185], v[38:41]
	v_mfma_f32_16x16x32_bf16 v[30:33], v[142:145], v[182:185], v[30:33]
	v_mfma_f32_16x16x32_bf16 v[22:25], v[134:137], v[196:199], v[22:25]
	v_mfma_f32_16x16x32_bf16 v[14:17], v[142:145], v[196:199], v[14:17]
	s_setprio 0
	s_setprio 1
	v_mfma_f32_16x16x32_bf16 v[50:53], v[146:149], v[162:165], v[50:53]
	v_mfma_f32_16x16x32_bf16 v[42:45], v[154:157], v[162:165], v[42:45]
	v_mfma_f32_16x16x32_bf16 v[34:37], v[146:149], v[170:173], v[34:37]
	v_mfma_f32_16x16x32_bf16 v[26:29], v[154:157], v[170:173], v[26:29]
	v_mfma_f32_16x16x32_bf16 v[18:21], v[146:149], v[178:181], v[18:21]
	v_mfma_f32_16x16x32_bf16 v[10:13], v[154:157], v[178:181], v[10:13]
	v_mfma_f32_16x16x32_bf16 v[6:9], v[146:149], v[192:195], v[6:9]
	v_mfma_f32_16x16x32_bf16 v[2:5], v[154:157], v[192:195], v[2:5]
	v_mfma_f32_16x16x32_bf16 v[50:53], v[150:153], v[166:169], v[50:53]
	v_mfma_f32_16x16x32_bf16 v[42:45], v[158:161], v[166:169], v[42:45]
	v_mfma_f32_16x16x32_bf16 v[34:37], v[150:153], v[174:177], v[34:37]
	v_mfma_f32_16x16x32_bf16 v[26:29], v[158:161], v[174:177], v[26:29]
	v_mfma_f32_16x16x32_bf16 v[18:21], v[150:153], v[182:185], v[18:21]
	v_mfma_f32_16x16x32_bf16 v[10:13], v[158:161], v[182:185], v[10:13]
	v_mfma_f32_16x16x32_bf16 v[6:9], v[150:153], v[196:199], v[6:9]
	v_mfma_f32_16x16x32_bf16 v[2:5], v[158:161], v[196:199], v[2:5]
	s_setprio 0
	s_barrier
	s_add_i32 s18, s18, 2
	s_add_u32 s5, s5, 0x100
	s_addc_u32 s15, s15, 0
	s_add_u32 s6, s6, 0x100
	s_addc_u32 s7, s7, 0
	s_cmp_gt_u32 s18, 29
	s_cbranch_scc0 .LBB0_115
	s_and_b64 vcc, exec, s[26:27]
	s_cbranch_vccz .LBB0_118
	s_barrier

.LBB0_793:
	s_add_u32 s0, s30, 0x80
	s_addc_u32 s1, s31, 0
	s_cmp_eq_u32 s55, 28
	s_cselect_b32 s35, s25, s1
	s_cselect_b32 s34, s24, s0
	s_cselect_b32 s1, s27, s23
	s_cselect_b32 s0, s26, s21
	v_mov_b32_e32 v130, v144
	s_add_i32 m0, s29, 0xc000
	s_nop 0
	global_load_lds_dwordx4 v130, s[30:31]
	v_mov_b32_e32 v130, v146
	s_add_i32 m0, s29, 0xe000
	s_nop 0
	global_load_lds_dwordx4 v130, s[30:31]
	ds_read_b128 v[136:139], v148
	ds_read_b128 v[152:155], v148 offset:1024
	ds_read_b128 v[156:159], v148 offset:2048
	ds_read_b128 v[160:163], v148 offset:3072
	ds_read_b128 v[164:167], v149
	ds_read_b128 v[168:171], v149 offset:1024
	ds_read_b128 v[172:175], v149 offset:2048
	ds_read_b128 v[176:179], v149 offset:3072
	ds_read_b128 v[180:183], v150
	ds_read_b128 v[184:187], v150 offset:1024
	ds_read_b128 v[188:191], v150 offset:2048
	ds_read_b128 v[192:195], v150 offset:3072
	ds_read_b128 v[196:199], v150 offset:4096
	ds_read_b128 v[200:203], v150 offset:5120
	ds_read_b128 v[204:207], v150 offset:6144
	ds_read_b128 v[208:211], v150 offset:7168
	s_waitcnt vmcnt(8)
	s_waitcnt lgkmcnt(0)
	s_barrier
	s_setprio 1
	s_waitcnt lgkmcnt(0)
	v_mfma_f32_16x16x32_bf16 v[126:129], v[136:139], v[180:183], v[126:129]
	v_mfma_f32_16x16x32_bf16 v[122:125], v[156:159], v[180:183], v[122:125]
	v_mfma_f32_16x16x32_bf16 v[118:121], v[136:139], v[188:191], v[118:121]
	v_mfma_f32_16x16x32_bf16 v[114:117], v[156:159], v[188:191], v[114:117]
	v_mfma_f32_16x16x32_bf16 v[110:113], v[136:139], v[196:199], v[110:113]
	v_mfma_f32_16x16x32_bf16 v[90:93], v[156:159], v[196:199], v[90:93]
	v_mfma_f32_16x16x32_bf16 v[82:85], v[136:139], v[204:207], v[82:85]
	v_mfma_f32_16x16x32_bf16 v[74:77], v[156:159], v[204:207], v[74:77]
	v_mfma_f32_16x16x32_bf16 v[126:129], v[152:155], v[184:187], v[126:129]
	v_mfma_f32_16x16x32_bf16 v[122:125], v[160:163], v[184:187], v[122:125]
	v_mfma_f32_16x16x32_bf16 v[118:121], v[152:155], v[192:195], v[118:121]
	v_mfma_f32_16x16x32_bf16 v[114:117], v[160:163], v[192:195], v[114:117]
	v_mfma_f32_16x16x32_bf16 v[110:113], v[152:155], v[200:203], v[110:113]
	v_mfma_f32_16x16x32_bf16 v[90:93], v[160:163], v[200:203], v[90:93]
	v_mfma_f32_16x16x32_bf16 v[82:85], v[152:155], v[208:211], v[82:85]
	v_mfma_f32_16x16x32_bf16 v[74:77], v[160:163], v[208:211], v[74:77]
	s_setprio 0
	s_setprio 1
	v_mfma_f32_16x16x32_bf16 v[106:109], v[164:167], v[180:183], v[106:109]
	v_mfma_f32_16x16x32_bf16 v[102:105], v[172:175], v[180:183], v[102:105]
	v_mfma_f32_16x16x32_bf16 v[98:101], v[164:167], v[188:191], v[98:101]
	v_mfma_f32_16x16x32_bf16 v[94:97], v[172:175], v[188:191], v[94:97]
	v_mfma_f32_16x16x32_bf16 v[86:89], v[164:167], v[196:199], v[86:89]
	v_mfma_f32_16x16x32_bf16 v[78:81], v[172:175], v[196:199], v[78:81]
	v_mfma_f32_16x16x32_bf16 v[70:73], v[164:167], v[204:207], v[70:73]
	v_mfma_f32_16x16x32_bf16 v[66:69], v[172:175], v[204:207], v[66:69]
	v_mfma_f32_16x16x32_bf16 v[106:109], v[168:171], v[184:187], v[106:109]
	v_mfma_f32_16x16x32_bf16 v[102:105], v[176:179], v[184:187], v[102:105]
	v_mfma_f32_16x16x32_bf16 v[98:101], v[168:171], v[192:195], v[98:101]
	v_mfma_f32_16x16x32_bf16 v[94:97], v[176:179], v[192:195], v[94:97]
	v_mfma_f32_16x16x32_bf16 v[86:89], v[168:171], v[200:203], v[86:89]
	v_mfma_f32_16x16x32_bf16 v[78:81], v[176:179], v[200:203], v[78:81]
	v_mfma_f32_16x16x32_bf16 v[70:73], v[168:171], v[208:211], v[70:73]
	v_mfma_f32_16x16x32_bf16 v[66:69], v[176:179], v[208:211], v[66:69]
	s_setprio 0
	s_barrier
	v_mov_b32_e32 v130, v1
	s_add_i32 s56, s50, s40
	s_mov_b32 m0, s56
	s_nop 0
	global_load_lds_dwordx4 v130, s[0:1]
	v_mov_b32_e32 v130, v142
	s_add_i32 m0, s56, 0x2000
	s_add_u32 s56, s0, 0x80000
	global_load_lds_dwordx4 v130, s[0:1]
	s_addc_u32 s57, s1, 0
	v_mov_b32_e32 v130, v1
	s_add_i32 s58, s51, s40
	s_mov_b32 m0, s58
	s_nop 0
	global_load_lds_dwordx4 v130, s[56:57]
	v_mov_b32_e32 v130, v142
	s_add_i32 m0, s58, 0x2000
	s_nop 0
	global_load_lds_dwordx4 v130, s[56:57]
	v_mov_b32_e32 v130, v143
	s_mov_b32 m0, s29
	s_nop 0
	global_load_lds_dwordx4 v130, s[34:35]
	v_mov_b32_e32 v130, v145
	s_mov_b32 m0, s41
	s_nop 0
	global_load_lds_dwordx4 v130, s[34:35]
	ds_read_b128 v[180:183], v150 offset:16384
	ds_read_b128 v[184:187], v150 offset:17408
	ds_read_b128 v[188:191], v150 offset:18432
	ds_read_b128 v[192:195], v150 offset:19456
	ds_read_b128 v[196:199], v150 offset:20480
	ds_read_b128 v[200:203], v150 offset:21504
	ds_read_b128 v[204:207], v150 offset:22528
	ds_read_b128 v[208:211], v150 offset:23552
	s_waitcnt vmcnt(8)
	s_waitcnt lgkmcnt(0)
	s_barrier
	s_setprio 1
	s_waitcnt lgkmcnt(0)
	v_mfma_f32_16x16x32_bf16 v[62:65], v[136:139], v[180:183], v[62:65]
	v_mfma_f32_16x16x32_bf16 v[58:61], v[156:159], v[180:183], v[58:61]
	v_mfma_f32_16x16x32_bf16 v[54:57], v[136:139], v[188:191], v[54:57]
	v_mfma_f32_16x16x32_bf16 v[50:53], v[156:159], v[188:191], v[50:53]
	v_mfma_f32_16x16x32_bf16 v[42:45], v[136:139], v[196:199], v[42:45]
	v_mfma_f32_16x16x32_bf16 v[34:37], v[156:159], v[196:199], v[34:37]
	v_mfma_f32_16x16x32_bf16 v[22:25], v[136:139], v[204:207], v[22:25]
	v_mfma_f32_16x16x32_bf16 v[10:13], v[156:159], v[204:207], v[10:13]
	v_mfma_f32_16x16x32_bf16 v[62:65], v[152:155], v[184:187], v[62:65]
	v_mfma_f32_16x16x32_bf16 v[58:61], v[160:163], v[184:187], v[58:61]
	v_mfma_f32_16x16x32_bf16 v[54:57], v[152:155], v[192:195], v[54:57]
	v_mfma_f32_16x16x32_bf16 v[50:53], v[160:163], v[192:195], v[50:53]
	v_mfma_f32_16x16x32_bf16 v[42:45], v[152:155], v[200:203], v[42:45]
	v_mfma_f32_16x16x32_bf16 v[34:37], v[160:163], v[200:203], v[34:37]
	v_mfma_f32_16x16x32_bf16 v[22:25], v[152:155], v[208:211], v[22:25]
	v_mfma_f32_16x16x32_bf16 v[10:13], v[160:163], v[208:211], v[10:13]
	s_setprio 0
	s_setprio 1
	v_mfma_f32_16x16x32_bf16 v[46:49], v[164:167], v[180:183], v[46:49]
	v_mfma_f32_16x16x32_bf16 v[38:41], v[172:175], v[180:183], v[38:41]
	v_mfma_f32_16x16x32_bf16 v[30:33], v[164:167], v[188:191], v[30:33]
	v_mfma_f32_16x16x32_bf16 v[26:29], v[172:175], v[188:191], v[26:29]
	v_mfma_f32_16x16x32_bf16 v[18:21], v[164:167], v[196:199], v[18:21]
	v_mfma_f32_16x16x32_bf16 v[14:17], v[172:175], v[196:199], v[14:17]
	v_mfma_f32_16x16x32_bf16 v[6:9], v[164:167], v[204:207], v[6:9]
	v_mfma_f32_16x16x32_bf16 v[2:5], v[172:175], v[204:207], v[2:5]
	v_mfma_f32_16x16x32_bf16 v[46:49], v[168:171], v[184:187], v[46:49]
	v_mfma_f32_16x16x32_bf16 v[38:41], v[176:179], v[184:187], v[38:41]
	v_mfma_f32_16x16x32_bf16 v[30:33], v[168:171], v[192:195], v[30:33]
	v_mfma_f32_16x16x32_bf16 v[26:29], v[176:179], v[192:195], v[26:29]
	v_mfma_f32_16x16x32_bf16 v[18:21], v[168:171], v[200:203], v[18:21]
	v_mfma_f32_16x16x32_bf16 v[14:17], v[176:179], v[200:203], v[14:17]
	v_mfma_f32_16x16x32_bf16 v[6:9], v[168:171], v[208:211], v[6:9]
	v_mfma_f32_16x16x32_bf16 v[2:5], v[176:179], v[208:211], v[2:5]
	s_setprio 0
	s_barrier
	s_add_i32 s56, 0, 0x18000
	v_add_u32_e32 v130, s56, v147
	s_add_i32 s57, 0, 0x1c000
	ds_read_b128 v[136:139], v130
	ds_read_b128 v[152:155], v130 offset:1024
	ds_read_b128 v[156:159], v130 offset:2048
	ds_read_b128 v[160:163], v130 offset:3072
	v_add_u32_e32 v130, s57, v147
	ds_read_b128 v[164:167], v130
	ds_read_b128 v[168:171], v130 offset:1024
	ds_read_b128 v[172:175], v130 offset:2048
	ds_read_b128 v[176:179], v130 offset:3072
	v_mov_b32_e32 v130, v144
	s_mov_b32 m0, s42
	ds_read_b128 v[180:183], v150 offset:32768
	ds_read_b128 v[184:187], v150 offset:33792
	ds_read_b128 v[188:191], v150 offset:34816
	ds_read_b128 v[192:195], v150 offset:35840
	ds_read_b128 v[196:199], v150 offset:36864
	ds_read_b128 v[200:203], v150 offset:37888
	ds_read_b128 v[204:207], v150 offset:38912
	ds_read_b128 v[208:211], v150 offset:39936
	s_nop 0
	global_load_lds_dwordx4 v130, s[34:35]
	v_mov_b32_e32 v130, v146
	s_mov_b32 m0, s43
	s_nop 0
	global_load_lds_dwordx4 v130, s[34:35]
	s_waitcnt vmcnt(8)
	s_waitcnt lgkmcnt(0)
	s_barrier
	s_setprio 1
	s_waitcnt lgkmcnt(0)
	v_mfma_f32_16x16x32_bf16 v[126:129], v[136:139], v[180:183], v[126:129]
	v_mfma_f32_16x16x32_bf16 v[122:125], v[156:159], v[180:183], v[122:125]
	v_mfma_f32_16x16x32_bf16 v[118:121], v[136:139], v[188:191], v[118:121]
	v_mfma_f32_16x16x32_bf16 v[114:117], v[156:159], v[188:191], v[114:117]
	v_mfma_f32_16x16x32_bf16 v[110:113], v[136:139], v[196:199], v[110:113]
	v_mfma_f32_16x16x32_bf16 v[90:93], v[156:159], v[196:199], v[90:93]
	v_mfma_f32_16x16x32_bf16 v[82:85], v[136:139], v[204:207], v[82:85]
	v_mfma_f32_16x16x32_bf16 v[74:77], v[156:159], v[204:207], v[74:77]
	v_mfma_f32_16x16x32_bf16 v[126:129], v[152:155], v[184:187], v[126:129]
	v_mfma_f32_16x16x32_bf16 v[122:125], v[160:163], v[184:187], v[122:125]
	v_mfma_f32_16x16x32_bf16 v[118:121], v[152:155], v[192:195], v[118:121]
	v_mfma_f32_16x16x32_bf16 v[114:117], v[160:163], v[192:195], v[114:117]
	v_mfma_f32_16x16x32_bf16 v[110:113], v[152:155], v[200:203], v[110:113]
	v_mfma_f32_16x16x32_bf16 v[90:93], v[160:163], v[200:203], v[90:93]
	v_mfma_f32_16x16x32_bf16 v[82:85], v[152:155], v[208:211], v[82:85]
	v_mfma_f32_16x16x32_bf16 v[74:77], v[160:163], v[208:211], v[74:77]
	s_setprio 0
	s_setprio 1
	v_mfma_f32_16x16x32_bf16 v[106:109], v[164:167], v[180:183], v[106:109]
	v_mfma_f32_16x16x32_bf16 v[102:105], v[172:175], v[180:183], v[102:105]
	v_mfma_f32_16x16x32_bf16 v[98:101], v[164:167], v[188:191], v[98:101]
	v_mfma_f32_16x16x32_bf16 v[94:97], v[172:175], v[188:191], v[94:97]
	v_mfma_f32_16x16x32_bf16 v[86:89], v[164:167], v[196:199], v[86:89]
	v_mfma_f32_16x16x32_bf16 v[78:81], v[172:175], v[196:199], v[78:81]
	v_mfma_f32_16x16x32_bf16 v[70:73], v[164:167], v[204:207], v[70:73]
	v_mfma_f32_16x16x32_bf16 v[66:69], v[172:175], v[204:207], v[66:69]
	v_mfma_f32_16x16x32_bf16 v[106:109], v[168:171], v[184:187], v[106:109]
	v_mfma_f32_16x16x32_bf16 v[102:105], v[176:179], v[184:187], v[102:105]
	v_mfma_f32_16x16x32_bf16 v[98:101], v[168:171], v[192:195], v[98:101]
	v_mfma_f32_16x16x32_bf16 v[94:97], v[176:179], v[192:195], v[94:97]
	v_mfma_f32_16x16x32_bf16 v[86:89], v[168:171], v[200:203], v[86:89]
	v_mfma_f32_16x16x32_bf16 v[78:81], v[176:179], v[200:203], v[78:81]
	v_mfma_f32_16x16x32_bf16 v[70:73], v[168:171], v[208:211], v[70:73]
	v_mfma_f32_16x16x32_bf16 v[66:69], v[176:179], v[208:211], v[66:69]
	s_setprio 0
	s_barrier
; template <class Epi, bool GATHER, bool EXPERT, bool FP8>
; DI void gemm_phase(LAS unsigned char* lds, const Gemm g, const StaticOrder& S, const Epi& E) {
;     ...
;         for (int t = 0; t < nt; t += 2) {
;             const bool last = (t == nt - 2);
;             const char* a1 = cA + (size_t)(t + 1) * kstep;
;             const char* a2 = last ? nA : cA + (size_t)(t + 2) * kstep; const char* b2 = last ? nB : cB + (size_t)(t + 2) * kstep;
;             const char* a3 = a2 + kstep; const char* b3 = b2 + kstep;
;             unsigned o00 = coffA[0][0], o01 = coffA[0][1], o10 = coffA[1][0], o11 = coffA[1][1];
;             if (GATHER && last && has_next) {
;                 o00 = sp[0] * (unsigned)(K * 2) + (unsigned)C0x2; o01 = sp[512] * (unsigned)(K * 2) + (unsigned)C1x2;
;                 o10 = sp[1024] * (unsigned)(K * 2) + (unsigned)C0x2; o11 = sp[1536] * (unsigned)(K * 2) + (unsigned)C1x2; }
;             PG8_TRIP(a1, a2, b2, a3, b3, o00, o01, o10, o11);
;             if (last) { coffA[0][0] = o00; coffA[0][1] = o01; coffA[1][0] = o10; coffA[1][1] = o11; }
;         }
	v_mov_b32_e32 v130, v1
	s_add_i32 s56, s56, s40
	v_lshl_add_u64 v[140:141], s[0:1], 0, v[130:131]
	v_lshl_add_u64 v[140:141], v[140:141], 0, s[68:69]
	s_mov_b32 m0, s56
	v_mov_b32_e32 v130, v142
	global_load_lds_dwordx4 v[140:141], off
	s_add_i32 m0, s56, 0x2000
	s_nop 0
	v_lshl_add_u64 v[140:141], s[0:1], 0, v[130:131]
	s_add_u32 s0, s0, 0x80080
	v_lshl_add_u64 v[140:141], v[140:141], 0, s[68:69]
	s_addc_u32 s1, s1, 0
	v_mov_b32_e32 v130, v1
	s_add_i32 s56, s57, s40
	global_load_lds_dwordx4 v[140:141], off
	s_mov_b32 m0, s56
	s_nop 0
	global_load_lds_dwordx4 v130, s[0:1]
	v_mov_b32_e32 v130, v142
	s_add_i32 m0, s56, 0x2000
	s_nop 0
	global_load_lds_dwordx4 v130, s[0:1]
	v_mov_b32_e32 v130, v143
	s_mov_b32 m0, s47
	v_lshl_add_u64 v[140:141], s[34:35], 0, v[130:131]
	v_lshl_add_u64 v[140:141], v[140:141], 0, s[68:69]
	v_mov_b32_e32 v130, v145
	global_load_lds_dwordx4 v[140:141], off
	s_mov_b32 m0, s48
	v_lshl_add_u64 v[140:141], s[34:35], 0, v[130:131]
	v_lshl_add_u64 v[140:141], v[140:141], 0, s[68:69]
	global_load_lds_dwordx4 v[140:141], off
	ds_read_b128 v[180:183], v150 offset:49152
	ds_read_b128 v[184:187], v150 offset:50176
	ds_read_b128 v[188:191], v150 offset:51200
	ds_read_b128 v[192:195], v150 offset:52224
	ds_read_b128 v[196:199], v150 offset:53248
	ds_read_b128 v[200:203], v150 offset:54272
	ds_read_b128 v[204:207], v150 offset:55296
	ds_read_b128 v[208:211], v150 offset:56320
	s_waitcnt vmcnt(8)
	s_waitcnt lgkmcnt(0)
	s_barrier
	s_setprio 1
	s_waitcnt lgkmcnt(0)
	v_mfma_f32_16x16x32_bf16 v[62:65], v[136:139], v[180:183], v[62:65]
	v_mfma_f32_16x16x32_bf16 v[58:61], v[156:159], v[180:183], v[58:61]
	v_mfma_f32_16x16x32_bf16 v[54:57], v[136:139], v[188:191], v[54:57]
	v_mfma_f32_16x16x32_bf16 v[50:53], v[156:159], v[188:191], v[50:53]
	v_mfma_f32_16x16x32_bf16 v[42:45], v[136:139], v[196:199], v[42:45]
	v_mfma_f32_16x16x32_bf16 v[34:37], v[156:159], v[196:199], v[34:37]
	v_mfma_f32_16x16x32_bf16 v[22:25], v[136:139], v[204:207], v[22:25]
	v_mfma_f32_16x16x32_bf16 v[10:13], v[156:159], v[204:207], v[10:13]
	v_mfma_f32_16x16x32_bf16 v[62:65], v[152:155], v[184:187], v[62:65]
	v_mfma_f32_16x16x32_bf16 v[58:61], v[160:163], v[184:187], v[58:61]
	v_mfma_f32_16x16x32_bf16 v[54:57], v[152:155], v[192:195], v[54:57]
	v_mfma_f32_16x16x32_bf16 v[50:53], v[160:163], v[192:195], v[50:53]
	v_mfma_f32_16x16x32_bf16 v[42:45], v[152:155], v[200:203], v[42:45]
	v_mfma_f32_16x16x32_bf16 v[34:37], v[160:163], v[200:203], v[34:37]
	v_mfma_f32_16x16x32_bf16 v[22:25], v[152:155], v[208:211], v[22:25]
	v_mfma_f32_16x16x32_bf16 v[10:13], v[160:163], v[208:211], v[10:13]
	s_setprio 0
	s_setprio 1
	v_mfma_f32_16x16x32_bf16 v[46:49], v[164:167], v[180:183], v[46:49]
	v_mfma_f32_16x16x32_bf16 v[38:41], v[172:175], v[180:183], v[38:41]
	v_mfma_f32_16x16x32_bf16 v[30:33], v[164:167], v[188:191], v[30:33]
	v_mfma_f32_16x16x32_bf16 v[26:29], v[172:175], v[188:191], v[26:29]
	v_mfma_f32_16x16x32_bf16 v[18:21], v[164:167], v[196:199], v[18:21]
	v_mfma_f32_16x16x32_bf16 v[14:17], v[172:175], v[196:199], v[14:17]
	v_mfma_f32_16x16x32_bf16 v[6:9], v[164:167], v[204:207], v[6:9]
	v_mfma_f32_16x16x32_bf16 v[2:5], v[172:175], v[204:207], v[2:5]
	v_mfma_f32_16x16x32_bf16 v[46:49], v[168:171], v[184:187], v[46:49]
	v_mfma_f32_16x16x32_bf16 v[38:41], v[176:179], v[184:187], v[38:41]
	v_mfma_f32_16x16x32_bf16 v[30:33], v[168:171], v[192:195], v[30:33]
	v_mfma_f32_16x16x32_bf16 v[26:29], v[176:179], v[192:195], v[26:29]
	v_mfma_f32_16x16x32_bf16 v[18:21], v[168:171], v[200:203], v[18:21]
	v_mfma_f32_16x16x32_bf16 v[14:17], v[176:179], v[200:203], v[14:17]
	v_mfma_f32_16x16x32_bf16 v[6:9], v[168:171], v[208:211], v[6:9]
	v_mfma_f32_16x16x32_bf16 v[2:5], v[176:179], v[208:211], v[2:5]
	s_setprio 0
	s_barrier
	s_add_i32 s55, s55, 2
	s_add_u32 s21, s21, 0x100
	s_addc_u32 s23, s23, 0
	s_add_u32 s30, s30, 0x100
	s_addc_u32 s31, s31, 0
	s_cmp_gt_u32 s55, 29
	s_cbranch_scc0 .LBB0_793
	s_and_b64 vcc, exec, s[72:73]
	s_cbranch_vccz .LBB0_796
	s_barrier

.LBB0_1087:
	v_add_u32_e32 v110, s67, v164
	ds_read_b128 v[168:171], v110
	ds_read_b128 v[172:175], v110 offset:1024
	ds_read_b128 v[176:179], v110 offset:2048
	ds_read_b128 v[180:183], v110 offset:3072
	v_add_u32_e32 v110, s68, v164
	ds_read_b128 v[184:187], v110
	ds_read_b128 v[188:191], v110 offset:1024
	ds_read_b128 v[192:195], v110 offset:2048
	ds_read_b128 v[196:199], v110 offset:3072
	s_add_u32 s1, s36, 0x80
	s_addc_u32 s42, s37, 0
	s_and_b64 s[40:41], s[38:39], exec
	s_cselect_b32 s41, s79, s42
	s_cselect_b32 s40, s78, s1
	s_cselect_b32 s43, s83, s72
	s_cselect_b32 s42, s82, s25
	v_mov_b32_e32 v110, v160
	ds_read_b128 v[200:203], v165
	ds_read_b128 v[204:207], v165 offset:1024
	ds_read_b128 v[208:211], v165 offset:2048
	ds_read_b128 v[212:215], v165 offset:3072
	ds_read_b128 v[216:219], v165 offset:4096
	ds_read_b128 v[220:223], v165 offset:5120
	ds_read_b128 v[226:229], v165 offset:6144
	ds_read_b128 v[230:233], v165 offset:7168
	s_add_i32 m0, s52, 0xc000
	s_nop 0
	global_load_lds_dwordx4 v110, s[36:37]
	v_mov_b32_e32 v110, v161
	s_add_i32 m0, s52, 0xe000
	s_nop 0
	global_load_lds_dwordx4 v110, s[36:37]
	s_waitcnt vmcnt(8)
	s_waitcnt lgkmcnt(0)
	s_barrier
	s_setprio 1
	s_waitcnt lgkmcnt(0)
	v_mfma_scale_f32_16x16x128_f8f6f4 v[114:117], v[168:175], v[208:215], v[114:117], v166, v166 op_sel_hi:[0,0,0]
	v_mfma_scale_f32_16x16x128_f8f6f4 v[102:105], v[176:183], v[208:215], v[102:105], v166, v166 op_sel_hi:[0,0,0]
	v_mfma_scale_f32_16x16x128_f8f6f4 v[94:97], v[168:175], v[216:223], v[94:97], v166, v166 op_sel_hi:[0,0,0]
	v_mfma_scale_f32_16x16x128_f8f6f4 v[86:89], v[176:183], v[216:223], v[86:89], v166, v166 op_sel_hi:[0,0,0]
	v_mfma_scale_f32_16x16x128_f8f6f4 v[78:81], v[168:175], v[226:233], v[78:81], v166, v166 op_sel_hi:[0,0,0]
	v_mfma_scale_f32_16x16x128_f8f6f4 v[70:73], v[176:183], v[226:233], v[70:73], v166, v166 op_sel_hi:[0,0,0]
	v_mfma_scale_f32_16x16x128_f8f6f4 v[110:113], v[168:175], v[200:207], v[142:145], v166, v166 op_sel_hi:[0,0,0]
	v_mfma_scale_f32_16x16x128_f8f6f4 v[118:121], v[176:183], v[200:207], v[134:137], v166, v166 op_sel_hi:[0,0,0]
	s_setprio 0
	s_setprio 1
	v_mfma_scale_f32_16x16x128_f8f6f4 v[122:125], v[192:199], v[200:207], v[122:125], v166, v166 op_sel_hi:[0,0,0]
	v_mfma_scale_f32_16x16x128_f8f6f4 v[106:109], v[184:191], v[208:215], v[106:109], v166, v166 op_sel_hi:[0,0,0]
	v_mfma_scale_f32_16x16x128_f8f6f4 v[98:101], v[192:199], v[208:215], v[98:101], v166, v166 op_sel_hi:[0,0,0]
	v_mfma_scale_f32_16x16x128_f8f6f4 v[90:93], v[184:191], v[216:223], v[90:93], v166, v166 op_sel_hi:[0,0,0]
	v_mfma_scale_f32_16x16x128_f8f6f4 v[82:85], v[192:199], v[216:223], v[82:85], v166, v166 op_sel_hi:[0,0,0]
	v_mfma_scale_f32_16x16x128_f8f6f4 v[74:77], v[184:191], v[226:233], v[74:77], v166, v166 op_sel_hi:[0,0,0]
	v_mfma_scale_f32_16x16x128_f8f6f4 v[66:69], v[192:199], v[226:233], v[66:69], v166, v166 op_sel_hi:[0,0,0]
	v_mfma_scale_f32_16x16x128_f8f6f4 v[126:129], v[184:191], v[200:207], v[138:141], v166, v166 op_sel_hi:[0,0,0]
	s_setprio 0
	s_barrier
	v_mov_b32_e32 v142, v158
	s_add_i32 s1, s67, s45
	s_nop 1
	s_mov_b32 m0, s1
	s_nop 0
	global_load_lds_dwordx4 v142, s[42:43]
	v_mov_b32_e32 v142, v159
	s_add_i32 m0, s1, 0x2000
	s_add_u32 s74, s42, 0x40000
	global_load_lds_dwordx4 v142, s[42:43]
	s_addc_u32 s75, s43, 0
	v_mov_b32_e32 v142, v158
	s_add_i32 s1, s68, s45
	s_mov_b32 m0, s1
	s_nop 0
	global_load_lds_dwordx4 v142, s[74:75]
	v_mov_b32_e32 v142, v159
	s_add_i32 m0, s1, 0x2000
	s_nop 0
	global_load_lds_dwordx4 v142, s[74:75]
	v_mov_b32_e32 v142, v133
	s_mov_b32 m0, s52
	s_nop 0
	global_load_lds_dwordx4 v142, s[40:41]
	v_mov_b32_e32 v142, v150
	s_mov_b32 m0, s53
	s_nop 0
	global_load_lds_dwordx4 v142, s[40:41]
	ds_read_b128 v[134:137], v165 offset:16384
	ds_read_b128 v[138:141], v165 offset:17408
	ds_read_b128 v[200:203], v165 offset:18432
	ds_read_b128 v[204:207], v165 offset:19456
	ds_read_b128 v[208:211], v165 offset:20480
	ds_read_b128 v[212:215], v165 offset:21504
	ds_read_b128 v[216:219], v165 offset:22528
	ds_read_b128 v[220:223], v165 offset:23552
	s_waitcnt vmcnt(8)
	s_waitcnt lgkmcnt(0)
	s_barrier
	s_setprio 1
	s_waitcnt lgkmcnt(0)
	v_mfma_scale_f32_16x16x128_f8f6f4 v[62:65], v[168:175], v[134:141], v[62:65], v166, v166 op_sel_hi:[0,0,0]
	v_mfma_scale_f32_16x16x128_f8f6f4 v[54:57], v[176:183], v[134:141], v[54:57], v166, v166 op_sel_hi:[0,0,0]
	v_mfma_scale_f32_16x16x128_f8f6f4 v[46:49], v[168:175], v[200:207], v[46:49], v166, v166 op_sel_hi:[0,0,0]
	v_mfma_scale_f32_16x16x128_f8f6f4 v[38:41], v[176:183], v[200:207], v[38:41], v166, v166 op_sel_hi:[0,0,0]
	v_mfma_scale_f32_16x16x128_f8f6f4 v[30:33], v[168:175], v[208:215], v[30:33], v166, v166 op_sel_hi:[0,0,0]
	v_mfma_scale_f32_16x16x128_f8f6f4 v[22:25], v[176:183], v[208:215], v[22:25], v166, v166 op_sel_hi:[0,0,0]
	v_mfma_scale_f32_16x16x128_f8f6f4 v[14:17], v[168:175], v[216:223], v[14:17], v166, v166 op_sel_hi:[0,0,0]
	v_mfma_scale_f32_16x16x128_f8f6f4 v[6:9], v[176:183], v[216:223], v[6:9], v166, v166 op_sel_hi:[0,0,0]
	s_setprio 0
	s_setprio 1
	v_mfma_scale_f32_16x16x128_f8f6f4 v[58:61], v[184:191], v[134:141], v[58:61], v166, v166 op_sel_hi:[0,0,0]
	v_mfma_scale_f32_16x16x128_f8f6f4 v[50:53], v[192:199], v[134:141], v[50:53], v166, v166 op_sel_hi:[0,0,0]
	v_mfma_scale_f32_16x16x128_f8f6f4 v[42:45], v[184:191], v[200:207], v[42:45], v166, v166 op_sel_hi:[0,0,0]
	v_mfma_scale_f32_16x16x128_f8f6f4 v[34:37], v[192:199], v[200:207], v[34:37], v166, v166 op_sel_hi:[0,0,0]
	v_mfma_scale_f32_16x16x128_f8f6f4 v[26:29], v[184:191], v[208:215], v[26:29], v166, v166 op_sel_hi:[0,0,0]
	v_mfma_scale_f32_16x16x128_f8f6f4 v[18:21], v[192:199], v[208:215], v[18:21], v166, v166 op_sel_hi:[0,0,0]
	v_mfma_scale_f32_16x16x128_f8f6f4 v[10:13], v[184:191], v[216:223], v[10:13], v166, v166 op_sel_hi:[0,0,0]
	v_mfma_scale_f32_16x16x128_f8f6f4 v[2:5], v[192:199], v[216:223], v[2:5], v166, v166 op_sel_hi:[0,0,0]
	s_setprio 0
	s_barrier
	s_add_i32 s1, 0, 0x18000
	v_add_u32_e32 v134, s1, v164
	s_add_i32 s73, 0, 0x1c000
	ds_read_b128 v[168:171], v134
	ds_read_b128 v[172:175], v134 offset:1024
	ds_read_b128 v[176:179], v134 offset:2048
	ds_read_b128 v[180:183], v134 offset:3072
	v_add_u32_e32 v134, s73, v164
	ds_read_b128 v[184:187], v134
	ds_read_b128 v[188:191], v134 offset:1024
	ds_read_b128 v[192:195], v134 offset:2048
	ds_read_b128 v[196:199], v134 offset:3072
	v_mov_b32_e32 v134, v151
	s_mov_b32 m0, s54
	ds_read_b128 v[200:203], v165 offset:32768
	ds_read_b128 v[204:207], v165 offset:33792
	ds_read_b128 v[208:211], v165 offset:34816
	ds_read_b128 v[212:215], v165 offset:35840
	ds_read_b128 v[216:219], v165 offset:36864
	ds_read_b128 v[220:223], v165 offset:37888
	ds_read_b128 v[226:229], v165 offset:38912
	ds_read_b128 v[230:233], v165 offset:39936
	s_nop 0
	global_load_lds_dwordx4 v134, s[40:41]
	v_mov_b32_e32 v134, v152
	s_mov_b32 m0, s55
	s_nop 0
	global_load_lds_dwordx4 v134, s[40:41]
	s_waitcnt vmcnt(8)
	s_waitcnt lgkmcnt(0)
	s_barrier
	s_setprio 1
	s_waitcnt lgkmcnt(0)
	v_mfma_scale_f32_16x16x128_f8f6f4 v[142:145], v[168:175], v[200:207], v[110:113], v166, v166 op_sel_hi:[0,0,0]
	v_mfma_scale_f32_16x16x128_f8f6f4 v[134:137], v[176:183], v[200:207], v[118:121], v166, v166 op_sel_hi:[0,0,0]
	v_mfma_scale_f32_16x16x128_f8f6f4 v[114:117], v[168:175], v[208:215], v[114:117], v166, v166 op_sel_hi:[0,0,0]
	v_mfma_scale_f32_16x16x128_f8f6f4 v[102:105], v[176:183], v[208:215], v[102:105], v166, v166 op_sel_hi:[0,0,0]
	v_mfma_scale_f32_16x16x128_f8f6f4 v[94:97], v[168:175], v[216:223], v[94:97], v166, v166 op_sel_hi:[0,0,0]
	v_mfma_scale_f32_16x16x128_f8f6f4 v[86:89], v[176:183], v[216:223], v[86:89], v166, v166 op_sel_hi:[0,0,0]
	v_mfma_scale_f32_16x16x128_f8f6f4 v[78:81], v[168:175], v[226:233], v[78:81], v166, v166 op_sel_hi:[0,0,0]
	v_mfma_scale_f32_16x16x128_f8f6f4 v[70:73], v[176:183], v[226:233], v[70:73], v166, v166 op_sel_hi:[0,0,0]
	s_setprio 0
	s_setprio 1
	v_mfma_scale_f32_16x16x128_f8f6f4 v[138:141], v[184:191], v[200:207], v[126:129], v166, v166 op_sel_hi:[0,0,0]
	v_mfma_scale_f32_16x16x128_f8f6f4 v[122:125], v[192:199], v[200:207], v[122:125], v166, v166 op_sel_hi:[0,0,0]
	v_mfma_scale_f32_16x16x128_f8f6f4 v[106:109], v[184:191], v[208:215], v[106:109], v166, v166 op_sel_hi:[0,0,0]
	v_mfma_scale_f32_16x16x128_f8f6f4 v[98:101], v[192:199], v[208:215], v[98:101], v166, v166 op_sel_hi:[0,0,0]
	v_mfma_scale_f32_16x16x128_f8f6f4 v[90:93], v[184:191], v[216:223], v[90:93], v166, v166 op_sel_hi:[0,0,0]
	v_mfma_scale_f32_16x16x128_f8f6f4 v[82:85], v[192:199], v[216:223], v[82:85], v166, v166 op_sel_hi:[0,0,0]
	v_mfma_scale_f32_16x16x128_f8f6f4 v[74:77], v[184:191], v[226:233], v[74:77], v166, v166 op_sel_hi:[0,0,0]
	v_mfma_scale_f32_16x16x128_f8f6f4 v[66:69], v[192:199], v[226:233], v[66:69], v166, v166 op_sel_hi:[0,0,0]
	s_setprio 0
	s_barrier
	v_mov_b32_e32 v146, v158
	s_add_i32 s1, s1, s45
	v_lshl_add_u64 v[110:111], s[42:43], 0, v[146:147]
	v_lshl_add_u64 v[110:111], v[110:111], 0, s[88:89]
	s_mov_b32 m0, s1
	v_mov_b32_e32 v146, v159
	global_load_lds_dwordx4 v[110:111], off
	s_add_i32 m0, s1, 0x2000
	v_lshl_add_u64 v[110:111], s[42:43], 0, v[146:147]
	v_lshl_add_u64 v[110:111], v[110:111], 0, s[88:89]
	s_add_u32 s42, s42, 0x40080
	global_load_lds_dwordx4 v[110:111], off
	s_addc_u32 s43, s43, 0
	v_mov_b32_e32 v110, v158
	s_add_i32 s1, s73, s45
	s_mov_b32 m0, s1
	v_mov_b32_e32 v146, v133
	global_load_lds_dwordx4 v110, s[42:43]
	v_mov_b32_e32 v110, v159
	s_add_i32 m0, s1, 0x2000
	s_nop 0
	global_load_lds_dwordx4 v110, s[42:43]
	s_mov_b32 m0, s59
	v_lshl_add_u64 v[110:111], s[40:41], 0, v[146:147]
	v_lshl_add_u64 v[110:111], v[110:111], 0, s[88:89]
	v_mov_b32_e32 v146, v150
	global_load_lds_dwordx4 v[110:111], off
	s_mov_b32 m0, s60
	v_lshl_add_u64 v[110:111], s[40:41], 0, v[146:147]
	v_lshl_add_u64 v[110:111], v[110:111], 0, s[88:89]
	global_load_lds_dwordx4 v[110:111], off
	ds_read_b128 v[200:203], v165 offset:49152
	ds_read_b128 v[204:207], v165 offset:50176
	ds_read_b128 v[208:211], v165 offset:51200
	ds_read_b128 v[212:215], v165 offset:52224
	ds_read_b128 v[216:219], v165 offset:53248
	ds_read_b128 v[220:223], v165 offset:54272
	ds_read_b128 v[226:229], v165 offset:55296
	ds_read_b128 v[230:233], v165 offset:56320
	s_waitcnt vmcnt(8)
	s_waitcnt lgkmcnt(0)
	s_barrier
	s_setprio 1
	s_waitcnt lgkmcnt(0)
	v_mfma_scale_f32_16x16x128_f8f6f4 v[62:65], v[168:175], v[200:207], v[62:65], v166, v166 op_sel_hi:[0,0,0]
	v_mfma_scale_f32_16x16x128_f8f6f4 v[54:57], v[176:183], v[200:207], v[54:57], v166, v166 op_sel_hi:[0,0,0]
	v_mfma_scale_f32_16x16x128_f8f6f4 v[46:49], v[168:175], v[208:215], v[46:49], v166, v166 op_sel_hi:[0,0,0]
	v_mfma_scale_f32_16x16x128_f8f6f4 v[38:41], v[176:183], v[208:215], v[38:41], v166, v166 op_sel_hi:[0,0,0]
	v_mfma_scale_f32_16x16x128_f8f6f4 v[30:33], v[168:175], v[216:223], v[30:33], v166, v166 op_sel_hi:[0,0,0]
	v_mfma_scale_f32_16x16x128_f8f6f4 v[22:25], v[176:183], v[216:223], v[22:25], v166, v166 op_sel_hi:[0,0,0]
	v_mfma_scale_f32_16x16x128_f8f6f4 v[14:17], v[168:175], v[226:233], v[14:17], v166, v166 op_sel_hi:[0,0,0]
	v_mfma_scale_f32_16x16x128_f8f6f4 v[6:9], v[176:183], v[226:233], v[6:9], v166, v166 op_sel_hi:[0,0,0]
	s_setprio 0
	s_setprio 1
	v_mfma_scale_f32_16x16x128_f8f6f4 v[58:61], v[184:191], v[200:207], v[58:61], v166, v166 op_sel_hi:[0,0,0]
	v_mfma_scale_f32_16x16x128_f8f6f4 v[50:53], v[192:199], v[200:207], v[50:53], v166, v166 op_sel_hi:[0,0,0]
	v_mfma_scale_f32_16x16x128_f8f6f4 v[42:45], v[184:191], v[208:215], v[42:45], v166, v166 op_sel_hi:[0,0,0]
	v_mfma_scale_f32_16x16x128_f8f6f4 v[34:37], v[192:199], v[208:215], v[34:37], v166, v166 op_sel_hi:[0,0,0]
	v_mfma_scale_f32_16x16x128_f8f6f4 v[26:29], v[184:191], v[216:223], v[26:29], v166, v166 op_sel_hi:[0,0,0]
	v_mfma_scale_f32_16x16x128_f8f6f4 v[18:21], v[192:199], v[216:223], v[18:21], v166, v166 op_sel_hi:[0,0,0]
	v_mfma_scale_f32_16x16x128_f8f6f4 v[10:13], v[184:191], v[226:233], v[10:13], v166, v166 op_sel_hi:[0,0,0]
	v_mfma_scale_f32_16x16x128_f8f6f4 v[2:5], v[192:199], v[226:233], v[2:5], v166, v166 op_sel_hi:[0,0,0]
	s_setprio 0
	s_barrier
	s_andn2_b64 vcc, exec, s[38:39]
	s_cbranch_vccnz .LBB0_1084
	v_mov_b32_e32 v161, v152
	v_mov_b32_e32 v160, v151
	v_mov_b32_e32 v163, v150
	v_mov_b32_e32 v162, v133
	s_branch .LBB0_1084

; template <class Epi, bool GATHER, bool EXPERT, bool FP8>
; DI void gemm_phase(LAS unsigned char* lds, const Gemm g, const StaticOrder& S, const Epi& E) {
;     ...
;             const bool last = (t == nt - 2);
;             const char* a1 = cA + (size_t)(t + 1) * kstep;
;             const char* a2 = last ? nA : cA + (size_t)(t + 2) * kstep; const char* b2 = last ? nB : cB + (size_t)(t + 2) * kstep;
;             const char* a3 = a2 + kstep; const char* b3 = b2 + kstep;
.LBB0_1161:
	s_add_u32 s23, s34, 0x80
	s_addc_u32 s33, s35, 0
	s_cmp_eq_u32 s21, 12
	s_cselect_b32 s37, s25, s33
	s_cselect_b32 s36, s24, s23
	s_cselect_b32 s39, s5, s1
	s_cselect_b32 s38, s4, s0
	v_mov_b32_e32 v144, v153
	s_add_i32 m0, s31, 0xc000
	s_nop 0
	global_load_lds_dwordx4 v144, s[34:35]
	v_mov_b32_e32 v144, v155
	s_add_i32 m0, s31, 0xe000
	s_nop 0
	global_load_lds_dwordx4 v144, s[34:35]
	ds_read_b128 v[128:131], v157
	ds_read_b128 v[132:135], v157 offset:1024
	ds_read_b128 v[136:139], v157 offset:2048
	ds_read_b128 v[140:143], v157 offset:3072
	ds_read_b128 v[162:165], v158
	ds_read_b128 v[166:169], v158 offset:1024
	ds_read_b128 v[170:173], v158 offset:2048
	ds_read_b128 v[174:177], v158 offset:3072
	ds_read_b128 v[178:181], v159
	ds_read_b128 v[182:185], v159 offset:1024
	ds_read_b128 v[186:189], v159 offset:2048
	ds_read_b128 v[190:193], v159 offset:3072
	ds_read_b128 v[194:197], v159 offset:4096
	ds_read_b128 v[198:201], v159 offset:5120
	ds_read_b128 v[202:205], v159 offset:6144
	ds_read_b128 v[206:209], v159 offset:7168
	s_waitcnt vmcnt(8)
	s_waitcnt lgkmcnt(0)
	s_barrier
	s_setprio 1
	s_waitcnt lgkmcnt(0)
	v_mfma_scale_f32_16x16x128_f8f6f4 v[124:127], v[128:135], v[178:185], v[124:127], v160, v160 op_sel_hi:[0,0,0]
	v_mfma_scale_f32_16x16x128_f8f6f4 v[120:123], v[136:143], v[178:185], v[120:123], v160, v160 op_sel_hi:[0,0,0]
	v_mfma_scale_f32_16x16x128_f8f6f4 v[116:119], v[128:135], v[186:193], v[116:119], v160, v160 op_sel_hi:[0,0,0]
	v_mfma_scale_f32_16x16x128_f8f6f4 v[112:115], v[136:143], v[186:193], v[112:115], v160, v160 op_sel_hi:[0,0,0]
	v_mfma_scale_f32_16x16x128_f8f6f4 v[210:213], v[128:135], v[194:201], v[92:95], v160, v160 op_sel_hi:[0,0,0]
	v_mfma_scale_f32_16x16x128_f8f6f4 v[214:217], v[136:143], v[194:201], v[88:91], v160, v160 op_sel_hi:[0,0,0]
	v_mfma_scale_f32_16x16x128_f8f6f4 v[218:221], v[128:135], v[202:209], v[84:87], v160, v160 op_sel_hi:[0,0,0]
	v_mfma_scale_f32_16x16x128_f8f6f4 v[226:229], v[136:143], v[202:209], v[80:83], v160, v160 op_sel_hi:[0,0,0]
	s_setprio 0
	s_setprio 1
	v_mfma_scale_f32_16x16x128_f8f6f4 v[108:111], v[162:169], v[178:185], v[108:111], v160, v160 op_sel_hi:[0,0,0]
	v_mfma_scale_f32_16x16x128_f8f6f4 v[104:107], v[170:177], v[178:185], v[104:107], v160, v160 op_sel_hi:[0,0,0]
	v_mfma_scale_f32_16x16x128_f8f6f4 v[100:103], v[162:169], v[186:193], v[100:103], v160, v160 op_sel_hi:[0,0,0]
	v_mfma_scale_f32_16x16x128_f8f6f4 v[96:99], v[170:177], v[186:193], v[96:99], v160, v160 op_sel_hi:[0,0,0]
	v_mfma_scale_f32_16x16x128_f8f6f4 v[230:233], v[162:169], v[194:201], v[76:79], v160, v160 op_sel_hi:[0,0,0]
	v_mfma_scale_f32_16x16x128_f8f6f4 v[194:197], v[170:177], v[194:201], v[72:75], v160, v160 op_sel_hi:[0,0,0]
	v_mfma_scale_f32_16x16x128_f8f6f4 v[198:201], v[162:169], v[202:209], v[68:71], v160, v160 op_sel_hi:[0,0,0]
	v_mfma_scale_f32_16x16x128_f8f6f4 v[202:205], v[170:177], v[202:209], v[64:67], v160, v160 op_sel_hi:[0,0,0]
	s_setprio 0
	s_barrier
	v_mov_b32_e32 v144, v150
	s_add_i32 s23, s57, s43
	s_nop 2
	s_mov_b32 m0, s23
	s_nop 0
	global_load_lds_dwordx4 v144, s[38:39]
	v_mov_b32_e32 v144, v151
	s_add_i32 m0, s23, 0x2000
	s_add_u32 s62, s38, 0x40000
	global_load_lds_dwordx4 v144, s[38:39]
	s_addc_u32 s63, s39, 0
	v_mov_b32_e32 v144, v150
	s_add_i32 s23, s58, s43
	s_mov_b32 m0, s23
	s_nop 0
	global_load_lds_dwordx4 v144, s[62:63]
	v_mov_b32_e32 v144, v151
	s_add_i32 m0, s23, 0x2000
	s_nop 0
	global_load_lds_dwordx4 v144, s[62:63]
	v_mov_b32_e32 v144, v152
	s_mov_b32 m0, s31
	s_nop 0
	global_load_lds_dwordx4 v144, s[36:37]
	v_mov_b32_e32 v144, v154
	s_mov_b32 m0, s49
	s_nop 0
	global_load_lds_dwordx4 v144, s[36:37]
	ds_read_b128 v[64:67], v159 offset:16384
	ds_read_b128 v[68:71], v159 offset:17408
	ds_read_b128 v[72:75], v159 offset:18432
	ds_read_b128 v[76:79], v159 offset:19456
	ds_read_b128 v[80:83], v159 offset:20480
	ds_read_b128 v[84:87], v159 offset:21504
	ds_read_b128 v[88:91], v159 offset:22528
	ds_read_b128 v[92:95], v159 offset:23552
	s_waitcnt vmcnt(8)
	s_waitcnt lgkmcnt(0)
	s_barrier
	s_setprio 1
	s_waitcnt lgkmcnt(0)
	v_mfma_scale_f32_16x16x128_f8f6f4 v[60:63], v[128:135], v[64:71], v[60:63], v160, v160 op_sel_hi:[0,0,0]
	v_mfma_scale_f32_16x16x128_f8f6f4 v[56:59], v[136:143], v[64:71], v[56:59], v160, v160 op_sel_hi:[0,0,0]
	v_mfma_scale_f32_16x16x128_f8f6f4 v[52:55], v[128:135], v[72:79], v[52:55], v160, v160 op_sel_hi:[0,0,0]
	v_mfma_scale_f32_16x16x128_f8f6f4 v[48:51], v[136:143], v[72:79], v[48:51], v160, v160 op_sel_hi:[0,0,0]
	v_mfma_scale_f32_16x16x128_f8f6f4 v[28:31], v[128:135], v[80:87], v[28:31], v160, v160 op_sel_hi:[0,0,0]
	v_mfma_scale_f32_16x16x128_f8f6f4 v[24:27], v[136:143], v[80:87], v[24:27], v160, v160 op_sel_hi:[0,0,0]
	v_mfma_scale_f32_16x16x128_f8f6f4 v[20:23], v[128:135], v[88:95], v[20:23], v160, v160 op_sel_hi:[0,0,0]
	v_mfma_scale_f32_16x16x128_f8f6f4 v[16:19], v[136:143], v[88:95], v[16:19], v160, v160 op_sel_hi:[0,0,0]
	s_setprio 0
	s_setprio 1
	v_mfma_scale_f32_16x16x128_f8f6f4 v[44:47], v[162:169], v[64:71], v[44:47], v160, v160 op_sel_hi:[0,0,0]
	v_mfma_scale_f32_16x16x128_f8f6f4 v[40:43], v[170:177], v[64:71], v[40:43], v160, v160 op_sel_hi:[0,0,0]
	v_mfma_scale_f32_16x16x128_f8f6f4 v[36:39], v[162:169], v[72:79], v[36:39], v160, v160 op_sel_hi:[0,0,0]
	v_mfma_scale_f32_16x16x128_f8f6f4 v[32:35], v[170:177], v[72:79], v[32:35], v160, v160 op_sel_hi:[0,0,0]
	v_mfma_scale_f32_16x16x128_f8f6f4 v[12:15], v[162:169], v[80:87], v[12:15], v160, v160 op_sel_hi:[0,0,0]
	v_mfma_scale_f32_16x16x128_f8f6f4 v[8:11], v[170:177], v[80:87], v[8:11], v160, v160 op_sel_hi:[0,0,0]
	v_mfma_scale_f32_16x16x128_f8f6f4 v[4:7], v[162:169], v[88:95], v[4:7], v160, v160 op_sel_hi:[0,0,0]
	v_mfma_scale_f32_16x16x128_f8f6f4 v[0:3], v[170:177], v[88:95], v[0:3], v160, v160 op_sel_hi:[0,0,0]
	s_setprio 0
	s_barrier
; template <class Epi, bool GATHER, bool EXPERT, bool FP8>
; DI void gemm_phase(LAS unsigned char* lds, const Gemm g, const StaticOrder& S, const Epi& E) {
;     ...
;         for (int t = 0; t < nt; t += 2) {
;             const bool last = (t == nt - 2);
;             const char* a1 = cA + (size_t)(t + 1) * kstep;
;             const char* a2 = last ? nA : cA + (size_t)(t + 2) * kstep; const char* b2 = last ? nB : cB + (size_t)(t + 2) * kstep;
;             const char* a3 = a2 + kstep; const char* b3 = b2 + kstep;
;             unsigned o00 = coffA[0][0], o01 = coffA[0][1], o10 = coffA[1][0], o11 = coffA[1][1];
;             if (GATHER && last && has_next) {
;                 o00 = sp[0] * (unsigned)(K * 2) + (unsigned)C0x2; o01 = sp[512] * (unsigned)(K * 2) + (unsigned)C1x2;
;                 o10 = sp[1024] * (unsigned)(K * 2) + (unsigned)C0x2; o11 = sp[1536] * (unsigned)(K * 2) + (unsigned)C1x2; }
;             PG8_TRIP(a1, a2, b2, a3, b3, o00, o01, o10, o11);
;             if (last) { coffA[0][0] = o00; coffA[0][1] = o01; coffA[1][0] = o10; coffA[1][1] = o11; }
;         }
	s_add_i32 s23, 0, 0x18000
	v_add_u32_e32 v64, s23, v156
	s_add_i32 s33, 0, 0x1c000
	ds_read_b128 v[128:131], v64
	ds_read_b128 v[132:135], v64 offset:1024
	ds_read_b128 v[136:139], v64 offset:2048
	ds_read_b128 v[140:143], v64 offset:3072
	v_add_u32_e32 v64, s33, v156
	ds_read_b128 v[162:165], v64
	ds_read_b128 v[166:169], v64 offset:1024
	ds_read_b128 v[170:173], v64 offset:2048
	ds_read_b128 v[174:177], v64 offset:3072
	v_mov_b32_e32 v80, v153
	s_mov_b32 m0, s50
	ds_read_b128 v[64:67], v159 offset:32768
	ds_read_b128 v[68:71], v159 offset:33792
	ds_read_b128 v[72:75], v159 offset:34816
	ds_read_b128 v[76:79], v159 offset:35840
	ds_read_b128 v[178:181], v159 offset:36864
	ds_read_b128 v[182:185], v159 offset:37888
	ds_read_b128 v[186:189], v159 offset:38912
	ds_read_b128 v[190:193], v159 offset:39936
	s_nop 0
	global_load_lds_dwordx4 v80, s[36:37]
	v_mov_b32_e32 v80, v155
	s_mov_b32 m0, s51
	s_nop 0
	global_load_lds_dwordx4 v80, s[36:37]
	s_waitcnt vmcnt(8)
	s_waitcnt lgkmcnt(0)
	s_barrier
	s_setprio 1
	s_waitcnt lgkmcnt(0)
	v_mfma_scale_f32_16x16x128_f8f6f4 v[124:127], v[128:135], v[64:71], v[124:127], v160, v160 op_sel_hi:[0,0,0]
	v_mfma_scale_f32_16x16x128_f8f6f4 v[120:123], v[136:143], v[64:71], v[120:123], v160, v160 op_sel_hi:[0,0,0]
	v_mfma_scale_f32_16x16x128_f8f6f4 v[116:119], v[128:135], v[72:79], v[116:119], v160, v160 op_sel_hi:[0,0,0]
	v_mfma_scale_f32_16x16x128_f8f6f4 v[112:115], v[136:143], v[72:79], v[112:115], v160, v160 op_sel_hi:[0,0,0]
	v_mfma_scale_f32_16x16x128_f8f6f4 v[92:95], v[128:135], v[178:185], v[210:213], v160, v160 op_sel_hi:[0,0,0]
	v_mfma_scale_f32_16x16x128_f8f6f4 v[88:91], v[136:143], v[178:185], v[214:217], v160, v160 op_sel_hi:[0,0,0]
	v_mfma_scale_f32_16x16x128_f8f6f4 v[84:87], v[128:135], v[186:193], v[218:221], v160, v160 op_sel_hi:[0,0,0]
	v_mfma_scale_f32_16x16x128_f8f6f4 v[80:83], v[136:143], v[186:193], v[226:229], v160, v160 op_sel_hi:[0,0,0]
	s_setprio 0
	s_setprio 1
	v_mfma_scale_f32_16x16x128_f8f6f4 v[108:111], v[162:169], v[64:71], v[108:111], v160, v160 op_sel_hi:[0,0,0]
	v_mfma_scale_f32_16x16x128_f8f6f4 v[104:107], v[170:177], v[64:71], v[104:107], v160, v160 op_sel_hi:[0,0,0]
	v_mfma_scale_f32_16x16x128_f8f6f4 v[100:103], v[162:169], v[72:79], v[100:103], v160, v160 op_sel_hi:[0,0,0]
	v_mfma_scale_f32_16x16x128_f8f6f4 v[96:99], v[170:177], v[72:79], v[96:99], v160, v160 op_sel_hi:[0,0,0]
	v_mfma_scale_f32_16x16x128_f8f6f4 v[76:79], v[162:169], v[178:185], v[230:233], v160, v160 op_sel_hi:[0,0,0]
	v_mfma_scale_f32_16x16x128_f8f6f4 v[72:75], v[170:177], v[178:185], v[194:197], v160, v160 op_sel_hi:[0,0,0]
	v_mfma_scale_f32_16x16x128_f8f6f4 v[68:71], v[162:169], v[186:193], v[198:201], v160, v160 op_sel_hi:[0,0,0]
	v_mfma_scale_f32_16x16x128_f8f6f4 v[64:67], v[170:177], v[186:193], v[202:205], v160, v160 op_sel_hi:[0,0,0]
	s_setprio 0
	s_barrier
	v_mov_b32_e32 v144, v150
	s_add_i32 s23, s23, s43
	v_lshl_add_u64 v[148:149], s[38:39], 0, v[144:145]
	v_lshl_add_u64 v[148:149], v[148:149], 0, s[14:15]
	s_mov_b32 m0, s23
	v_mov_b32_e32 v144, v151
	global_load_lds_dwordx4 v[148:149], off
	s_add_i32 m0, s23, 0x2000
	s_nop 0
	v_lshl_add_u64 v[148:149], s[38:39], 0, v[144:145]
	s_add_u32 s38, s38, 0x40080
	v_lshl_add_u64 v[148:149], v[148:149], 0, s[14:15]
	s_addc_u32 s39, s39, 0
	v_mov_b32_e32 v144, v150
	s_add_i32 s23, s33, s43
	global_load_lds_dwordx4 v[148:149], off
	s_mov_b32 m0, s23
	s_nop 0
	global_load_lds_dwordx4 v144, s[38:39]
	v_mov_b32_e32 v144, v151
	s_add_i32 m0, s23, 0x2000
	s_nop 0
	global_load_lds_dwordx4 v144, s[38:39]
	v_mov_b32_e32 v144, v152
	s_mov_b32 m0, s52
	v_lshl_add_u64 v[148:149], s[36:37], 0, v[144:145]
	v_lshl_add_u64 v[148:149], v[148:149], 0, s[14:15]
	v_mov_b32_e32 v144, v154
	global_load_lds_dwordx4 v[148:149], off
	s_mov_b32 m0, s53
	v_lshl_add_u64 v[148:149], s[36:37], 0, v[144:145]
	v_lshl_add_u64 v[148:149], v[148:149], 0, s[14:15]
	global_load_lds_dwordx4 v[148:149], off
	ds_read_b128 v[178:181], v159 offset:49152
	ds_read_b128 v[182:185], v159 offset:50176
	ds_read_b128 v[186:189], v159 offset:51200
	ds_read_b128 v[190:193], v159 offset:52224
	ds_read_b128 v[194:197], v159 offset:53248
	ds_read_b128 v[198:201], v159 offset:54272
	ds_read_b128 v[202:205], v159 offset:55296
	ds_read_b128 v[206:209], v159 offset:56320
	s_waitcnt vmcnt(8)
	s_waitcnt lgkmcnt(0)
	s_barrier
	s_setprio 1
	s_waitcnt lgkmcnt(0)
	v_mfma_scale_f32_16x16x128_f8f6f4 v[60:63], v[128:135], v[178:185], v[60:63], v160, v160 op_sel_hi:[0,0,0]
	v_mfma_scale_f32_16x16x128_f8f6f4 v[56:59], v[136:143], v[178:185], v[56:59], v160, v160 op_sel_hi:[0,0,0]
	v_mfma_scale_f32_16x16x128_f8f6f4 v[52:55], v[128:135], v[186:193], v[52:55], v160, v160 op_sel_hi:[0,0,0]
	v_mfma_scale_f32_16x16x128_f8f6f4 v[48:51], v[136:143], v[186:193], v[48:51], v160, v160 op_sel_hi:[0,0,0]
	v_mfma_scale_f32_16x16x128_f8f6f4 v[28:31], v[128:135], v[194:201], v[28:31], v160, v160 op_sel_hi:[0,0,0]
	v_mfma_scale_f32_16x16x128_f8f6f4 v[24:27], v[136:143], v[194:201], v[24:27], v160, v160 op_sel_hi:[0,0,0]
	v_mfma_scale_f32_16x16x128_f8f6f4 v[20:23], v[128:135], v[202:209], v[20:23], v160, v160 op_sel_hi:[0,0,0]
	v_mfma_scale_f32_16x16x128_f8f6f4 v[16:19], v[136:143], v[202:209], v[16:19], v160, v160 op_sel_hi:[0,0,0]
	s_setprio 0
	s_setprio 1
	v_mfma_scale_f32_16x16x128_f8f6f4 v[44:47], v[162:169], v[178:185], v[44:47], v160, v160 op_sel_hi:[0,0,0]
	v_mfma_scale_f32_16x16x128_f8f6f4 v[40:43], v[170:177], v[178:185], v[40:43], v160, v160 op_sel_hi:[0,0,0]
	v_mfma_scale_f32_16x16x128_f8f6f4 v[36:39], v[162:169], v[186:193], v[36:39], v160, v160 op_sel_hi:[0,0,0]
	v_mfma_scale_f32_16x16x128_f8f6f4 v[32:35], v[170:177], v[186:193], v[32:35], v160, v160 op_sel_hi:[0,0,0]
	v_mfma_scale_f32_16x16x128_f8f6f4 v[12:15], v[162:169], v[194:201], v[12:15], v160, v160 op_sel_hi:[0,0,0]
	v_mfma_scale_f32_16x16x128_f8f6f4 v[8:11], v[170:177], v[194:201], v[8:11], v160, v160 op_sel_hi:[0,0,0]
	v_mfma_scale_f32_16x16x128_f8f6f4 v[4:7], v[162:169], v[202:209], v[4:7], v160, v160 op_sel_hi:[0,0,0]
	v_mfma_scale_f32_16x16x128_f8f6f4 v[0:3], v[170:177], v[202:209], v[0:3], v160, v160 op_sel_hi:[0,0,0]
	s_setprio 0
	s_barrier
	s_add_i32 s21, s21, 2
	s_add_u32 s0, s0, 0x100
	s_addc_u32 s1, s1, 0
	s_add_u32 s34, s34, 0x100
	s_addc_u32 s35, s35, 0
	s_cmp_gt_u32 s21, 13
	s_cbranch_scc0 .LBB0_1161
	s_and_b64 vcc, exec, s[16:17]
	s_cbranch_vccz .LBB0_1164
	s_barrier
